# mLSTM phase AB: u' block with batched LDS reads and packed FMAs
# baseline (speedup 1.0000x reference)
.LBB0_510:
	s_add_i32 s82, s80, 0
	s_add_i32 s22, s82, 0x14000
	v_mov_b32_e32 v2, s22
	ds_read2_b32 v[96:97], v2 offset1:1
	s_add_i32 s81, s79, 0
	v_mov_b32_e32 v136, 0
	s_and_saveexec_b64 s[46:47], s[16:17]
	s_cbranch_execz .LBB0_512
	s_add_i32 s22, s81, 0x10000
	v_mov_b32_e32 v176, s22
	ds_read_b128 v[180:183], v132 offset:9216
	ds_read_b128 v[184:187], v132 offset:9232
	ds_read_b128 v[188:191], v132 offset:9248
	ds_read_b128 v[192:195], v132 offset:9264
	ds_read_b128 v[196:199], v132 offset:9280
	ds_read_b128 v[200:203], v132 offset:9296
	ds_read_b128 v[204:207], v132 offset:9312
	ds_read_b128 v[208:211], v132 offset:9328
	ds_read_b128 v[212:215], v176 offset:0
	ds_read_b128 v[216:219], v176 offset:16
	ds_read_b128 v[220:223], v176 offset:32
	ds_read_b128 v[224:227], v176 offset:48
	ds_read_b128 v[228:231], v176 offset:64
	ds_read_b128 v[232:235], v176 offset:80
	ds_read_b128 v[236:239], v176 offset:96
	ds_read_b128 v[240:243], v176 offset:112
	s_waitcnt lgkmcnt(0)
	v_lshlrev_b32_e32 v244, 16, v180
	v_and_b32_e32 v245, 0xffff0000, v180
	v_pk_mul_f32 v[178:179], v[244:245], v[212:213]
	v_lshlrev_b32_e32 v244, 16, v181
	v_and_b32_e32 v245, 0xffff0000, v181
	v_pk_fma_f32 v[178:179], v[244:245], v[214:215], v[178:179]
	v_lshlrev_b32_e32 v244, 16, v182
	v_and_b32_e32 v245, 0xffff0000, v182
	v_pk_fma_f32 v[178:179], v[244:245], v[216:217], v[178:179]
	v_lshlrev_b32_e32 v244, 16, v183
	v_and_b32_e32 v245, 0xffff0000, v183
	v_pk_fma_f32 v[178:179], v[244:245], v[218:219], v[178:179]
	v_lshlrev_b32_e32 v244, 16, v184
	v_and_b32_e32 v245, 0xffff0000, v184
	v_pk_fma_f32 v[178:179], v[244:245], v[220:221], v[178:179]
	v_lshlrev_b32_e32 v244, 16, v185
	v_and_b32_e32 v245, 0xffff0000, v185
	v_pk_fma_f32 v[178:179], v[244:245], v[222:223], v[178:179]
	v_lshlrev_b32_e32 v244, 16, v186
	v_and_b32_e32 v245, 0xffff0000, v186
	v_pk_fma_f32 v[178:179], v[244:245], v[224:225], v[178:179]
	v_lshlrev_b32_e32 v244, 16, v187
	v_and_b32_e32 v245, 0xffff0000, v187
	v_pk_fma_f32 v[178:179], v[244:245], v[226:227], v[178:179]
	ds_read_b128 v[212:215], v176 offset:128
	ds_read_b128 v[216:219], v176 offset:144
	ds_read_b128 v[220:223], v176 offset:160
	ds_read_b128 v[224:227], v176 offset:176
	v_lshlrev_b32_e32 v244, 16, v188
	v_and_b32_e32 v245, 0xffff0000, v188
	v_pk_fma_f32 v[178:179], v[244:245], v[228:229], v[178:179]
	v_lshlrev_b32_e32 v244, 16, v189
	v_and_b32_e32 v245, 0xffff0000, v189
	v_pk_fma_f32 v[178:179], v[244:245], v[230:231], v[178:179]
	v_lshlrev_b32_e32 v244, 16, v190
	v_and_b32_e32 v245, 0xffff0000, v190
	v_pk_fma_f32 v[178:179], v[244:245], v[232:233], v[178:179]
	v_lshlrev_b32_e32 v244, 16, v191
	v_and_b32_e32 v245, 0xffff0000, v191
	v_pk_fma_f32 v[178:179], v[244:245], v[234:235], v[178:179]
	v_lshlrev_b32_e32 v244, 16, v192
	v_and_b32_e32 v245, 0xffff0000, v192
	v_pk_fma_f32 v[178:179], v[244:245], v[236:237], v[178:179]
	v_lshlrev_b32_e32 v244, 16, v193
	v_and_b32_e32 v245, 0xffff0000, v193
	v_pk_fma_f32 v[178:179], v[244:245], v[238:239], v[178:179]
	v_lshlrev_b32_e32 v244, 16, v194
	v_and_b32_e32 v245, 0xffff0000, v194
	v_pk_fma_f32 v[178:179], v[244:245], v[240:241], v[178:179]
	v_lshlrev_b32_e32 v244, 16, v195
	v_and_b32_e32 v245, 0xffff0000, v195
	v_pk_fma_f32 v[178:179], v[244:245], v[242:243], v[178:179]
	ds_read_b128 v[228:231], v176 offset:192
	ds_read_b128 v[232:235], v176 offset:208
	ds_read_b128 v[236:239], v176 offset:224
	ds_read_b128 v[240:243], v176 offset:240
	s_waitcnt lgkmcnt(4)
	v_lshlrev_b32_e32 v244, 16, v196
	v_and_b32_e32 v245, 0xffff0000, v196
	v_pk_fma_f32 v[178:179], v[244:245], v[212:213], v[178:179]
	v_lshlrev_b32_e32 v244, 16, v197
	v_and_b32_e32 v245, 0xffff0000, v197
	v_pk_fma_f32 v[178:179], v[244:245], v[214:215], v[178:179]
	v_lshlrev_b32_e32 v244, 16, v198
	v_and_b32_e32 v245, 0xffff0000, v198
	v_pk_fma_f32 v[178:179], v[244:245], v[216:217], v[178:179]
	v_lshlrev_b32_e32 v244, 16, v199
	v_and_b32_e32 v245, 0xffff0000, v199
	v_pk_fma_f32 v[178:179], v[244:245], v[218:219], v[178:179]
	v_lshlrev_b32_e32 v244, 16, v200
	v_and_b32_e32 v245, 0xffff0000, v200
	v_pk_fma_f32 v[178:179], v[244:245], v[220:221], v[178:179]
	v_lshlrev_b32_e32 v244, 16, v201
	v_and_b32_e32 v245, 0xffff0000, v201
	v_pk_fma_f32 v[178:179], v[244:245], v[222:223], v[178:179]
	v_lshlrev_b32_e32 v244, 16, v202
	v_and_b32_e32 v245, 0xffff0000, v202
	v_pk_fma_f32 v[178:179], v[244:245], v[224:225], v[178:179]
	v_lshlrev_b32_e32 v244, 16, v203
	v_and_b32_e32 v245, 0xffff0000, v203
	v_pk_fma_f32 v[178:179], v[244:245], v[226:227], v[178:179]
	s_waitcnt lgkmcnt(0)
	v_lshlrev_b32_e32 v244, 16, v204
	v_and_b32_e32 v245, 0xffff0000, v204
	v_pk_fma_f32 v[178:179], v[244:245], v[228:229], v[178:179]
	v_lshlrev_b32_e32 v244, 16, v205
	v_and_b32_e32 v245, 0xffff0000, v205
	v_pk_fma_f32 v[178:179], v[244:245], v[230:231], v[178:179]
	v_lshlrev_b32_e32 v244, 16, v206
	v_and_b32_e32 v245, 0xffff0000, v206
	v_pk_fma_f32 v[178:179], v[244:245], v[232:233], v[178:179]
	v_lshlrev_b32_e32 v244, 16, v207
	v_and_b32_e32 v245, 0xffff0000, v207
	v_pk_fma_f32 v[178:179], v[244:245], v[234:235], v[178:179]
	v_lshlrev_b32_e32 v244, 16, v208
	v_and_b32_e32 v245, 0xffff0000, v208
	v_pk_fma_f32 v[178:179], v[244:245], v[236:237], v[178:179]
	v_lshlrev_b32_e32 v244, 16, v209
	v_and_b32_e32 v245, 0xffff0000, v209
	v_pk_fma_f32 v[178:179], v[244:245], v[238:239], v[178:179]
	v_lshlrev_b32_e32 v244, 16, v210
	v_and_b32_e32 v245, 0xffff0000, v210
	v_pk_fma_f32 v[178:179], v[244:245], v[240:241], v[178:179]
	v_lshlrev_b32_e32 v244, 16, v211
	v_and_b32_e32 v245, 0xffff0000, v211
	v_pk_fma_f32 v[178:179], v[244:245], v[242:243], v[178:179]
	v_add_f32_e32 v136, v178, v179

.LBB0_520:
	s_add_i32 s22, s82, 0x14008
	v_mov_b32_e32 v94, s22
	ds_read2_b32 v[94:95], v94 offset1:1
	v_mov_b32_e32 v135, 0
	s_and_saveexec_b64 s[46:47], s[16:17]
	s_cbranch_execz .LBB0_522
	s_add_i32 s22, s81, 0x10100
	v_mov_b32_e32 v176, s22
	ds_read_b128 v[180:183], v132 offset:37888
	ds_read_b128 v[184:187], v132 offset:37904
	ds_read_b128 v[188:191], v132 offset:37920
	ds_read_b128 v[192:195], v132 offset:37936
	ds_read_b128 v[196:199], v132 offset:37952
	ds_read_b128 v[200:203], v132 offset:37968
	ds_read_b128 v[204:207], v132 offset:37984
	ds_read_b128 v[208:211], v132 offset:38000
	ds_read_b128 v[212:215], v176 offset:0
	ds_read_b128 v[216:219], v176 offset:16
	ds_read_b128 v[220:223], v176 offset:32
	ds_read_b128 v[224:227], v176 offset:48
	ds_read_b128 v[228:231], v176 offset:64
	ds_read_b128 v[232:235], v176 offset:80
	ds_read_b128 v[236:239], v176 offset:96
	ds_read_b128 v[240:243], v176 offset:112
	s_waitcnt lgkmcnt(0)
	v_lshlrev_b32_e32 v244, 16, v180
	v_and_b32_e32 v245, 0xffff0000, v180
	v_pk_mul_f32 v[178:179], v[244:245], v[212:213]
	v_lshlrev_b32_e32 v244, 16, v181
	v_and_b32_e32 v245, 0xffff0000, v181
	v_pk_fma_f32 v[178:179], v[244:245], v[214:215], v[178:179]
	v_lshlrev_b32_e32 v244, 16, v182
	v_and_b32_e32 v245, 0xffff0000, v182
	v_pk_fma_f32 v[178:179], v[244:245], v[216:217], v[178:179]
	v_lshlrev_b32_e32 v244, 16, v183
	v_and_b32_e32 v245, 0xffff0000, v183
	v_pk_fma_f32 v[178:179], v[244:245], v[218:219], v[178:179]
	v_lshlrev_b32_e32 v244, 16, v184
	v_and_b32_e32 v245, 0xffff0000, v184
	v_pk_fma_f32 v[178:179], v[244:245], v[220:221], v[178:179]
	v_lshlrev_b32_e32 v244, 16, v185
	v_and_b32_e32 v245, 0xffff0000, v185
	v_pk_fma_f32 v[178:179], v[244:245], v[222:223], v[178:179]
	v_lshlrev_b32_e32 v244, 16, v186
	v_and_b32_e32 v245, 0xffff0000, v186
	v_pk_fma_f32 v[178:179], v[244:245], v[224:225], v[178:179]
	v_lshlrev_b32_e32 v244, 16, v187
	v_and_b32_e32 v245, 0xffff0000, v187
	v_pk_fma_f32 v[178:179], v[244:245], v[226:227], v[178:179]
	ds_read_b128 v[212:215], v176 offset:128
	ds_read_b128 v[216:219], v176 offset:144
	ds_read_b128 v[220:223], v176 offset:160
	ds_read_b128 v[224:227], v176 offset:176
	v_lshlrev_b32_e32 v244, 16, v188
	v_and_b32_e32 v245, 0xffff0000, v188
	v_pk_fma_f32 v[178:179], v[244:245], v[228:229], v[178:179]
	v_lshlrev_b32_e32 v244, 16, v189
	v_and_b32_e32 v245, 0xffff0000, v189
	v_pk_fma_f32 v[178:179], v[244:245], v[230:231], v[178:179]
	v_lshlrev_b32_e32 v244, 16, v190
	v_and_b32_e32 v245, 0xffff0000, v190
	v_pk_fma_f32 v[178:179], v[244:245], v[232:233], v[178:179]
	v_lshlrev_b32_e32 v244, 16, v191
	v_and_b32_e32 v245, 0xffff0000, v191
	v_pk_fma_f32 v[178:179], v[244:245], v[234:235], v[178:179]
	v_lshlrev_b32_e32 v244, 16, v192
	v_and_b32_e32 v245, 0xffff0000, v192
	v_pk_fma_f32 v[178:179], v[244:245], v[236:237], v[178:179]
	v_lshlrev_b32_e32 v244, 16, v193
	v_and_b32_e32 v245, 0xffff0000, v193
	v_pk_fma_f32 v[178:179], v[244:245], v[238:239], v[178:179]
	v_lshlrev_b32_e32 v244, 16, v194
	v_and_b32_e32 v245, 0xffff0000, v194
	v_pk_fma_f32 v[178:179], v[244:245], v[240:241], v[178:179]
	v_lshlrev_b32_e32 v244, 16, v195
	v_and_b32_e32 v245, 0xffff0000, v195
	v_pk_fma_f32 v[178:179], v[244:245], v[242:243], v[178:179]
	ds_read_b128 v[228:231], v176 offset:192
	ds_read_b128 v[232:235], v176 offset:208
	ds_read_b128 v[236:239], v176 offset:224
	ds_read_b128 v[240:243], v176 offset:240
	s_waitcnt lgkmcnt(4)
	v_lshlrev_b32_e32 v244, 16, v196
	v_and_b32_e32 v245, 0xffff0000, v196
	v_pk_fma_f32 v[178:179], v[244:245], v[212:213], v[178:179]
	v_lshlrev_b32_e32 v244, 16, v197
	v_and_b32_e32 v245, 0xffff0000, v197
	v_pk_fma_f32 v[178:179], v[244:245], v[214:215], v[178:179]
	v_lshlrev_b32_e32 v244, 16, v198
	v_and_b32_e32 v245, 0xffff0000, v198
	v_pk_fma_f32 v[178:179], v[244:245], v[216:217], v[178:179]
	v_lshlrev_b32_e32 v244, 16, v199
	v_and_b32_e32 v245, 0xffff0000, v199
	v_pk_fma_f32 v[178:179], v[244:245], v[218:219], v[178:179]
	v_lshlrev_b32_e32 v244, 16, v200
	v_and_b32_e32 v245, 0xffff0000, v200
	v_pk_fma_f32 v[178:179], v[244:245], v[220:221], v[178:179]
	v_lshlrev_b32_e32 v244, 16, v201
	v_and_b32_e32 v245, 0xffff0000, v201
	v_pk_fma_f32 v[178:179], v[244:245], v[222:223], v[178:179]
	v_lshlrev_b32_e32 v244, 16, v202
	v_and_b32_e32 v245, 0xffff0000, v202
	v_pk_fma_f32 v[178:179], v[244:245], v[224:225], v[178:179]
	v_lshlrev_b32_e32 v244, 16, v203
	v_and_b32_e32 v245, 0xffff0000, v203
	v_pk_fma_f32 v[178:179], v[244:245], v[226:227], v[178:179]
	s_waitcnt lgkmcnt(0)
	v_lshlrev_b32_e32 v244, 16, v204
	v_and_b32_e32 v245, 0xffff0000, v204
	v_pk_fma_f32 v[178:179], v[244:245], v[228:229], v[178:179]
	v_lshlrev_b32_e32 v244, 16, v205
	v_and_b32_e32 v245, 0xffff0000, v205
	v_pk_fma_f32 v[178:179], v[244:245], v[230:231], v[178:179]
	v_lshlrev_b32_e32 v244, 16, v206
	v_and_b32_e32 v245, 0xffff0000, v206
	v_pk_fma_f32 v[178:179], v[244:245], v[232:233], v[178:179]
	v_lshlrev_b32_e32 v244, 16, v207
	v_and_b32_e32 v245, 0xffff0000, v207
	v_pk_fma_f32 v[178:179], v[244:245], v[234:235], v[178:179]
	v_lshlrev_b32_e32 v244, 16, v208
	v_and_b32_e32 v245, 0xffff0000, v208
	v_pk_fma_f32 v[178:179], v[244:245], v[236:237], v[178:179]
	v_lshlrev_b32_e32 v244, 16, v209
	v_and_b32_e32 v245, 0xffff0000, v209
	v_pk_fma_f32 v[178:179], v[244:245], v[238:239], v[178:179]
	v_lshlrev_b32_e32 v244, 16, v210
	v_and_b32_e32 v245, 0xffff0000, v210
	v_pk_fma_f32 v[178:179], v[244:245], v[240:241], v[178:179]
	v_lshlrev_b32_e32 v244, 16, v211
	v_and_b32_e32 v245, 0xffff0000, v211
	v_pk_fma_f32 v[178:179], v[244:245], v[242:243], v[178:179]
	v_add_f32_e32 v135, v178, v179

.LBB0_530:
	s_add_i32 s22, s82, 0x14010
	v_mov_b32_e32 v78, s22
	ds_read2_b32 v[78:79], v78 offset1:1
	v_mov_b32_e32 v134, 0
	s_and_saveexec_b64 s[46:47], s[16:17]
	s_cbranch_execz .LBB0_532
	s_add_i32 s22, s81, 0x10200
	v_mov_b32_e32 v176, s22
	ds_read_b128 v[180:183], v132 offset:9216
	ds_read_b128 v[184:187], v132 offset:9232
	ds_read_b128 v[188:191], v132 offset:9248
	ds_read_b128 v[192:195], v132 offset:9264
	ds_read_b128 v[196:199], v132 offset:9280
	ds_read_b128 v[200:203], v132 offset:9296
	ds_read_b128 v[204:207], v132 offset:9312
	ds_read_b128 v[208:211], v132 offset:9328
	ds_read_b128 v[212:215], v176 offset:0
	ds_read_b128 v[216:219], v176 offset:16
	ds_read_b128 v[220:223], v176 offset:32
	ds_read_b128 v[224:227], v176 offset:48
	ds_read_b128 v[228:231], v176 offset:64
	ds_read_b128 v[232:235], v176 offset:80
	ds_read_b128 v[236:239], v176 offset:96
	ds_read_b128 v[240:243], v176 offset:112
	s_waitcnt lgkmcnt(0)
	v_lshlrev_b32_e32 v244, 16, v180
	v_and_b32_e32 v245, 0xffff0000, v180
	v_pk_mul_f32 v[178:179], v[244:245], v[212:213]
	v_lshlrev_b32_e32 v244, 16, v181
	v_and_b32_e32 v245, 0xffff0000, v181
	v_pk_fma_f32 v[178:179], v[244:245], v[214:215], v[178:179]
	v_lshlrev_b32_e32 v244, 16, v182
	v_and_b32_e32 v245, 0xffff0000, v182
	v_pk_fma_f32 v[178:179], v[244:245], v[216:217], v[178:179]
	v_lshlrev_b32_e32 v244, 16, v183
	v_and_b32_e32 v245, 0xffff0000, v183
	v_pk_fma_f32 v[178:179], v[244:245], v[218:219], v[178:179]
	v_lshlrev_b32_e32 v244, 16, v184
	v_and_b32_e32 v245, 0xffff0000, v184
	v_pk_fma_f32 v[178:179], v[244:245], v[220:221], v[178:179]
	v_lshlrev_b32_e32 v244, 16, v185
	v_and_b32_e32 v245, 0xffff0000, v185
	v_pk_fma_f32 v[178:179], v[244:245], v[222:223], v[178:179]
	v_lshlrev_b32_e32 v244, 16, v186
	v_and_b32_e32 v245, 0xffff0000, v186
	v_pk_fma_f32 v[178:179], v[244:245], v[224:225], v[178:179]
	v_lshlrev_b32_e32 v244, 16, v187
	v_and_b32_e32 v245, 0xffff0000, v187
	v_pk_fma_f32 v[178:179], v[244:245], v[226:227], v[178:179]
	ds_read_b128 v[212:215], v176 offset:128
	ds_read_b128 v[216:219], v176 offset:144
	ds_read_b128 v[220:223], v176 offset:160
	ds_read_b128 v[224:227], v176 offset:176
	v_lshlrev_b32_e32 v244, 16, v188
	v_and_b32_e32 v245, 0xffff0000, v188
	v_pk_fma_f32 v[178:179], v[244:245], v[228:229], v[178:179]
	v_lshlrev_b32_e32 v244, 16, v189
	v_and_b32_e32 v245, 0xffff0000, v189
	v_pk_fma_f32 v[178:179], v[244:245], v[230:231], v[178:179]
	v_lshlrev_b32_e32 v244, 16, v190
	v_and_b32_e32 v245, 0xffff0000, v190
	v_pk_fma_f32 v[178:179], v[244:245], v[232:233], v[178:179]
	v_lshlrev_b32_e32 v244, 16, v191
	v_and_b32_e32 v245, 0xffff0000, v191
	v_pk_fma_f32 v[178:179], v[244:245], v[234:235], v[178:179]
	v_lshlrev_b32_e32 v244, 16, v192
	v_and_b32_e32 v245, 0xffff0000, v192
	v_pk_fma_f32 v[178:179], v[244:245], v[236:237], v[178:179]
	v_lshlrev_b32_e32 v244, 16, v193
	v_and_b32_e32 v245, 0xffff0000, v193
	v_pk_fma_f32 v[178:179], v[244:245], v[238:239], v[178:179]
	v_lshlrev_b32_e32 v244, 16, v194
	v_and_b32_e32 v245, 0xffff0000, v194
	v_pk_fma_f32 v[178:179], v[244:245], v[240:241], v[178:179]
	v_lshlrev_b32_e32 v244, 16, v195
	v_and_b32_e32 v245, 0xffff0000, v195
	v_pk_fma_f32 v[178:179], v[244:245], v[242:243], v[178:179]
	ds_read_b128 v[228:231], v176 offset:192
	ds_read_b128 v[232:235], v176 offset:208
	ds_read_b128 v[236:239], v176 offset:224
	ds_read_b128 v[240:243], v176 offset:240
	s_waitcnt lgkmcnt(4)
	v_lshlrev_b32_e32 v244, 16, v196
	v_and_b32_e32 v245, 0xffff0000, v196
	v_pk_fma_f32 v[178:179], v[244:245], v[212:213], v[178:179]
	v_lshlrev_b32_e32 v244, 16, v197
	v_and_b32_e32 v245, 0xffff0000, v197
	v_pk_fma_f32 v[178:179], v[244:245], v[214:215], v[178:179]
	v_lshlrev_b32_e32 v244, 16, v198
	v_and_b32_e32 v245, 0xffff0000, v198
	v_pk_fma_f32 v[178:179], v[244:245], v[216:217], v[178:179]
	v_lshlrev_b32_e32 v244, 16, v199
	v_and_b32_e32 v245, 0xffff0000, v199
	v_pk_fma_f32 v[178:179], v[244:245], v[218:219], v[178:179]
	v_lshlrev_b32_e32 v244, 16, v200
	v_and_b32_e32 v245, 0xffff0000, v200
	v_pk_fma_f32 v[178:179], v[244:245], v[220:221], v[178:179]
	v_lshlrev_b32_e32 v244, 16, v201
	v_and_b32_e32 v245, 0xffff0000, v201
	v_pk_fma_f32 v[178:179], v[244:245], v[222:223], v[178:179]
	v_lshlrev_b32_e32 v244, 16, v202
	v_and_b32_e32 v245, 0xffff0000, v202
	v_pk_fma_f32 v[178:179], v[244:245], v[224:225], v[178:179]
	v_lshlrev_b32_e32 v244, 16, v203
	v_and_b32_e32 v245, 0xffff0000, v203
	v_pk_fma_f32 v[178:179], v[244:245], v[226:227], v[178:179]
	s_waitcnt lgkmcnt(0)
	v_lshlrev_b32_e32 v244, 16, v204
	v_and_b32_e32 v245, 0xffff0000, v204
	v_pk_fma_f32 v[178:179], v[244:245], v[228:229], v[178:179]
	v_lshlrev_b32_e32 v244, 16, v205
	v_and_b32_e32 v245, 0xffff0000, v205
	v_pk_fma_f32 v[178:179], v[244:245], v[230:231], v[178:179]
	v_lshlrev_b32_e32 v244, 16, v206
	v_and_b32_e32 v245, 0xffff0000, v206
	v_pk_fma_f32 v[178:179], v[244:245], v[232:233], v[178:179]
	v_lshlrev_b32_e32 v244, 16, v207
	v_and_b32_e32 v245, 0xffff0000, v207
	v_pk_fma_f32 v[178:179], v[244:245], v[234:235], v[178:179]
	v_lshlrev_b32_e32 v244, 16, v208
	v_and_b32_e32 v245, 0xffff0000, v208
	v_pk_fma_f32 v[178:179], v[244:245], v[236:237], v[178:179]
	v_lshlrev_b32_e32 v244, 16, v209
	v_and_b32_e32 v245, 0xffff0000, v209
	v_pk_fma_f32 v[178:179], v[244:245], v[238:239], v[178:179]
	v_lshlrev_b32_e32 v244, 16, v210
	v_and_b32_e32 v245, 0xffff0000, v210
	v_pk_fma_f32 v[178:179], v[244:245], v[240:241], v[178:179]
	v_lshlrev_b32_e32 v244, 16, v211
	v_and_b32_e32 v245, 0xffff0000, v211
	v_pk_fma_f32 v[178:179], v[244:245], v[242:243], v[178:179]
	v_add_f32_e32 v134, v178, v179

.LBB0_540:
	s_add_i32 s22, s82, 0x14018
	v_mov_b32_e32 v96, s22
	ds_read2_b32 v[96:97], v96 offset1:1
	v_mov_b32_e32 v99, 0
	s_and_saveexec_b64 s[46:47], s[16:17]
	s_cbranch_execz .LBB0_542
	s_add_i32 s22, s81, 0x10300
	v_mov_b32_e32 v176, s22
	ds_read_b128 v[180:183], v132 offset:37888
	ds_read_b128 v[184:187], v132 offset:37904
	ds_read_b128 v[188:191], v132 offset:37920
	ds_read_b128 v[192:195], v132 offset:37936
	ds_read_b128 v[196:199], v132 offset:37952
	ds_read_b128 v[200:203], v132 offset:37968
	ds_read_b128 v[204:207], v132 offset:37984
	ds_read_b128 v[208:211], v132 offset:38000
	ds_read_b128 v[212:215], v176 offset:0
	ds_read_b128 v[216:219], v176 offset:16
	ds_read_b128 v[220:223], v176 offset:32
	ds_read_b128 v[224:227], v176 offset:48
	ds_read_b128 v[228:231], v176 offset:64
	ds_read_b128 v[232:235], v176 offset:80
	ds_read_b128 v[236:239], v176 offset:96
	ds_read_b128 v[240:243], v176 offset:112
	s_waitcnt lgkmcnt(0)
	v_lshlrev_b32_e32 v244, 16, v180
	v_and_b32_e32 v245, 0xffff0000, v180
	v_pk_mul_f32 v[178:179], v[244:245], v[212:213]
	v_lshlrev_b32_e32 v244, 16, v181
	v_and_b32_e32 v245, 0xffff0000, v181
	v_pk_fma_f32 v[178:179], v[244:245], v[214:215], v[178:179]
	v_lshlrev_b32_e32 v244, 16, v182
	v_and_b32_e32 v245, 0xffff0000, v182
	v_pk_fma_f32 v[178:179], v[244:245], v[216:217], v[178:179]
	v_lshlrev_b32_e32 v244, 16, v183
	v_and_b32_e32 v245, 0xffff0000, v183
	v_pk_fma_f32 v[178:179], v[244:245], v[218:219], v[178:179]
	v_lshlrev_b32_e32 v244, 16, v184
	v_and_b32_e32 v245, 0xffff0000, v184
	v_pk_fma_f32 v[178:179], v[244:245], v[220:221], v[178:179]
	v_lshlrev_b32_e32 v244, 16, v185
	v_and_b32_e32 v245, 0xffff0000, v185
	v_pk_fma_f32 v[178:179], v[244:245], v[222:223], v[178:179]
	v_lshlrev_b32_e32 v244, 16, v186
	v_and_b32_e32 v245, 0xffff0000, v186
	v_pk_fma_f32 v[178:179], v[244:245], v[224:225], v[178:179]
	v_lshlrev_b32_e32 v244, 16, v187
	v_and_b32_e32 v245, 0xffff0000, v187
	v_pk_fma_f32 v[178:179], v[244:245], v[226:227], v[178:179]
	ds_read_b128 v[212:215], v176 offset:128
	ds_read_b128 v[216:219], v176 offset:144
	ds_read_b128 v[220:223], v176 offset:160
	ds_read_b128 v[224:227], v176 offset:176
	v_lshlrev_b32_e32 v244, 16, v188
	v_and_b32_e32 v245, 0xffff0000, v188
	v_pk_fma_f32 v[178:179], v[244:245], v[228:229], v[178:179]
	v_lshlrev_b32_e32 v244, 16, v189
	v_and_b32_e32 v245, 0xffff0000, v189
	v_pk_fma_f32 v[178:179], v[244:245], v[230:231], v[178:179]
	v_lshlrev_b32_e32 v244, 16, v190
	v_and_b32_e32 v245, 0xffff0000, v190
	v_pk_fma_f32 v[178:179], v[244:245], v[232:233], v[178:179]
	v_lshlrev_b32_e32 v244, 16, v191
	v_and_b32_e32 v245, 0xffff0000, v191
	v_pk_fma_f32 v[178:179], v[244:245], v[234:235], v[178:179]
	v_lshlrev_b32_e32 v244, 16, v192
	v_and_b32_e32 v245, 0xffff0000, v192
	v_pk_fma_f32 v[178:179], v[244:245], v[236:237], v[178:179]
	v_lshlrev_b32_e32 v244, 16, v193
	v_and_b32_e32 v245, 0xffff0000, v193
	v_pk_fma_f32 v[178:179], v[244:245], v[238:239], v[178:179]
	v_lshlrev_b32_e32 v244, 16, v194
	v_and_b32_e32 v245, 0xffff0000, v194
	v_pk_fma_f32 v[178:179], v[244:245], v[240:241], v[178:179]
	v_lshlrev_b32_e32 v244, 16, v195
	v_and_b32_e32 v245, 0xffff0000, v195
	v_pk_fma_f32 v[178:179], v[244:245], v[242:243], v[178:179]
	ds_read_b128 v[228:231], v176 offset:192
	ds_read_b128 v[232:235], v176 offset:208
	ds_read_b128 v[236:239], v176 offset:224
	ds_read_b128 v[240:243], v176 offset:240
	s_waitcnt lgkmcnt(4)
	v_lshlrev_b32_e32 v244, 16, v196
	v_and_b32_e32 v245, 0xffff0000, v196
	v_pk_fma_f32 v[178:179], v[244:245], v[212:213], v[178:179]
	v_lshlrev_b32_e32 v244, 16, v197
	v_and_b32_e32 v245, 0xffff0000, v197
	v_pk_fma_f32 v[178:179], v[244:245], v[214:215], v[178:179]
	v_lshlrev_b32_e32 v244, 16, v198
	v_and_b32_e32 v245, 0xffff0000, v198
	v_pk_fma_f32 v[178:179], v[244:245], v[216:217], v[178:179]
	v_lshlrev_b32_e32 v244, 16, v199
	v_and_b32_e32 v245, 0xffff0000, v199
	v_pk_fma_f32 v[178:179], v[244:245], v[218:219], v[178:179]
	v_lshlrev_b32_e32 v244, 16, v200
	v_and_b32_e32 v245, 0xffff0000, v200
	v_pk_fma_f32 v[178:179], v[244:245], v[220:221], v[178:179]
	v_lshlrev_b32_e32 v244, 16, v201
	v_and_b32_e32 v245, 0xffff0000, v201
	v_pk_fma_f32 v[178:179], v[244:245], v[222:223], v[178:179]
	v_lshlrev_b32_e32 v244, 16, v202
	v_and_b32_e32 v245, 0xffff0000, v202
	v_pk_fma_f32 v[178:179], v[244:245], v[224:225], v[178:179]
	v_lshlrev_b32_e32 v244, 16, v203
	v_and_b32_e32 v245, 0xffff0000, v203
	v_pk_fma_f32 v[178:179], v[244:245], v[226:227], v[178:179]
	s_waitcnt lgkmcnt(0)
	v_lshlrev_b32_e32 v244, 16, v204
	v_and_b32_e32 v245, 0xffff0000, v204
	v_pk_fma_f32 v[178:179], v[244:245], v[228:229], v[178:179]
	v_lshlrev_b32_e32 v244, 16, v205
	v_and_b32_e32 v245, 0xffff0000, v205
	v_pk_fma_f32 v[178:179], v[244:245], v[230:231], v[178:179]
	v_lshlrev_b32_e32 v244, 16, v206
	v_and_b32_e32 v245, 0xffff0000, v206
	v_pk_fma_f32 v[178:179], v[244:245], v[232:233], v[178:179]
	v_lshlrev_b32_e32 v244, 16, v207
	v_and_b32_e32 v245, 0xffff0000, v207
	v_pk_fma_f32 v[178:179], v[244:245], v[234:235], v[178:179]
	v_lshlrev_b32_e32 v244, 16, v208
	v_and_b32_e32 v245, 0xffff0000, v208
	v_pk_fma_f32 v[178:179], v[244:245], v[236:237], v[178:179]
	v_lshlrev_b32_e32 v244, 16, v209
	v_and_b32_e32 v245, 0xffff0000, v209
	v_pk_fma_f32 v[178:179], v[244:245], v[238:239], v[178:179]
	v_lshlrev_b32_e32 v244, 16, v210
	v_and_b32_e32 v245, 0xffff0000, v210
	v_pk_fma_f32 v[178:179], v[244:245], v[240:241], v[178:179]
	v_lshlrev_b32_e32 v244, 16, v211
	v_and_b32_e32 v245, 0xffff0000, v211
	v_pk_fma_f32 v[178:179], v[244:245], v[242:243], v[178:179]
	v_add_f32_e32 v99, v178, v179
